# gate_up epilogue bias loads issued at the top of the unit's last K-loop trip (plain trips), epilogue keeps its drain wait
# baseline (speedup 1.0000x reference)
;     __device__ __forceinline__ void operator()(const f32x4 (&acc)[2][2][4][2], const Unit& u, int wr, int wc, int fr, int fq) const {
;         const int row0 = u.pm * BM + wr * 64 + fr, cc = u.pn * HALF + wc * 32 + 8 * fq;
;         const float* bp = bias + (size_t)u.e * 4096 + cc;
;         f32x4 bg[2], bu[2];
; #pragma unroll
;         for (int n = 0; n < 2; ++n) { bg[n] = *(const f32x4*)(bp + 4 * n); bu[n] = *(const f32x4*)(bp + 2048 + 4 * n); }
.LBB0_853:
	v_mov_b32_e32 v18, v0
	s_lshl_b32 s0, s36, 7
	v_lshrrev_b32_e32 v2, 1, v18
	s_ashr_i32 s35, s34, 31
	v_and_or_b32 v2, v2, 24, s0
	s_lshl_b64 s[0:1], s[34:35], 14
	v_or_b32_e32 v20, s77, v2
	s_add_u32 s0, s48, s0
	s_addc_u32 s1, s49, s1
	v_ashrrev_i32_e32 v21, 31, v20
	v_lshl_add_u64 v[2:3], v[20:21], 2, s[0:1]
	s_cmp_eq_u32 s82, 4
	s_cbranch_scc1 .Lbp_pre
	global_load_dwordx4 v[14:17], v[2:3], off
	global_load_dwordx4 v[6:9], v[2:3], off offset:16
	v_add_co_u32_e32 v4, vcc, s56, v2
	v_and_or_b32 v18, v18, 15, s76
	s_nop 0
	v_addc_co_u32_e32 v5, vcc, 0, v3, vcc
	v_lshl_add_u64 v[2:3], v[2:3], 0, s[14:15]
	global_load_dwordx4 v[10:13], v[4:5], off
	v_lshl_add_u32 v22, s24, 8, v18
	global_load_dwordx4 v[2:5], v[2:3], off offset:16
	s_mov_b32 s34, s16
	s_mov_b32 s36, s18
	s_mov_b32 s24, s81
	s_mov_b64 s[0:1], s[20:21]
	s_lshr_b32 s90, s98, 1
	s_mul_i32 s90, s90, s83
	s_add_i32 s90, s90, s84
	s_cmp_lt_u32 s90, 0x8000
	s_cbranch_scc0 .Lesj_no
	s_lshr_b32 s91, s90, 10
	s_lshl_b32 s91, s91, 11
	s_and_b32 s99, s90, 0x3c0
	s_lshl_b32 s99, s99, 1
	s_or_b32 s91, s91, s99
	s_and_b32 s99, s98, 1
	s_lshl_b32 s99, s99, 6
	s_or_b32 s91, s91, s99
	s_and_b32 s90, s90, 63
	s_or_b32 s90, s90, s91
	s_lshr_b32 s91, s90, 11
	s_and_b32 s99, s90, 0x7c0
	s_and_b32 s82, s90, 63
	s_lshl_b32 s32, s91, 24
	s_lshl_b32 s100, s99, 13
	s_add_i32 s32, s32, s100
	s_lshl_b32 s100, s82, 7
	s_add_i32 s32, s32, s100
	s_add_u32 s100, s86, s32
	s_addc_u32 s101, s87, 0
	s_lshl_b32 s32, s91, 22
	s_lshl_b32 s82, s82, 16
	s_add_i32 s32, s32, s82
	s_add_i32 s32, s32, s99
	s_add_u32 s90, s88, s32
	s_addc_u32 s91, s89, 0
	global_load_dwordx4 v[218:221], v252, s[100:101] nt
	s_add_u32 s100, s100, 0x2000
	s_addc_u32 s101, s101, 0
	global_load_dwordx4 v[222:225], v252, s[100:101] nt
	s_add_u32 s100, s100, 0x2000
	s_addc_u32 s101, s101, 0
	global_load_dwordx4 v[226:229], v252, s[100:101] nt
	s_add_u32 s100, s100, 0x2000
	s_addc_u32 s101, s101, 0
	global_load_dwordx4 v[230:233], v252, s[100:101] nt
	s_add_u32 s100, s100, 0x2000
	s_addc_u32 s101, s101, 0
	global_load_dwordx4 v[234:237], v252, s[100:101] nt
	s_add_u32 s100, s100, 0x2000
	s_addc_u32 s101, s101, 0
	global_load_dwordx4 v[238:241], v252, s[100:101] nt
	s_add_u32 s100, s100, 0x2000
	s_addc_u32 s101, s101, 0
	global_load_dwordx4 v[242:245], v252, s[100:101] nt
	s_add_u32 s100, s100, 0x2000
	s_addc_u32 s101, s101, 0
	global_load_dwordx4 v[246:249], v252, s[100:101] nt
	s_mov_b32 s82, 1
	s_waitcnt vmcnt(8)
	s_branch .Lesj_join

; #define PG8_ROWS(x0, uidx) do { ro[x0] = (unsigned)g.rowtab[(uidx) * 256 + Rl + 64 * (x0)]; ro[(x0) + 1] = (unsigned)g.rowtab[(uidx) * 256 + Rl + 64 * (x0) + 64]; } while (0)
; #define PG8_LDA(dst, b, h) do { _Pragma("unroll") for (int m = 0; m < 4; ++m) { \
;         if constexpr (FP8) dst##8[m] = ld32(lds + PG8_SA(b, h) + aoff0 + m * 2048); \
;         else { dst[m][0] = *(const LAS bf16x8*)(lds + PG8_SA(b, h) + aoff0 + m * 2048); dst[m][1] = *(const LAS bf16x8*)(lds + PG8_SA(b, h) + aoff0 + m * 2048 + 1024); } } } while (0)
; #define PG8_LDB(dst, b, h) do { _Pragma("unroll") for (int n = 0; n < 2; ++n) { \
;         if constexpr (FP8) dst##8[n] = ld32(lds + PG8_SB(b, h) + boff0 + n * 2048); \
;         else { dst[n][0] = *(const LAS bf16x8*)(lds + PG8_SB(b, h) + boff0 + n * 2048); dst[n][1] = *(const LAS bf16x8*)(lds + PG8_SB(b, h) + boff0 + n * 2048 + 1024); } } } while (0)
; #define PG8_WAIT_V(n) asm volatile("s_waitcnt vmcnt(" #n ")" ::: "memory")
; #define PG8_WAIT_L(n) asm volatile("s_waitcnt lgkmcnt(" #n ")" ::: "memory")
; #define PG8_BAR __builtin_amdgcn_s_barrier()
; #define PG8_SCHED __builtin_amdgcn_sched_barrier(0)
; template <bool FP8, bool GATHER, class Epi, class Sched>
; __device__ __forceinline__ void gemm_phase(LAS unsigned char* lds, const Gemm g, const Sched& S, const Epi& E) {
;     ...
;         for (int t = 0; t < nt; t += 2) {
;             const bool last = (t == nt - 2);
;             const size_t k1 = (size_t)(t + 1) * kstep, k2 = last ? 0 : (size_t)(t + 2) * kstep, k3 = k2 + kstep;
;             const char* b2 = last ? nB : cB + (size_t)(t + 2) * kstep; const char* b3 = b2 + kstep;
;             if constexpr (GATHER) { if (last && has_next) PG8_ROWS(0, ui + 1); }
;             PG8_LDB(B0, 0, 0); PG8_SCHED; PG8_LDA(At, 0, 0); PG8_STAGEA(PG8_SA(1, 1), false, 1, k1);
;             if constexpr (GATHER) { if (last && has_next) PG8_ROWS(2, ui + 1); }
;             PG8_WAIT_V(10); PG8_WAIT_L(8); PG8_BAR; PG8_WAIT_L(0); PG8_MMA(0, 0, At, B0); PG8_BAR; PG8_SCHED;
.LBB0_865:
	s_cmp_eq_u32 s82, 2
	s_cbranch_scc1 .Lcj_865
	s_cmp_lg_u32 s85, 0
	s_cbranch_scc1 .Lsj_865
	s_cmp_eq_u32 s29, 12
	s_cbranch_scc1 .Llj_865
	s_cmp_eq_u32 s29, 12
	s_cselect_b64 s[42:43], -1, 0
	s_and_b64 s[30:31], s[38:39], s[42:43]
	v_cndmask_b32_e64 v2, 0, 1, s[30:31]
	v_cmp_ne_u32_e64 s[0:1], 1, v2
	s_andn2_b64 vcc, exec, s[30:31]
	s_cbranch_vccnz .LBB0_867
	ds_read2st64_b32 v[182:183], v199 offset1:1

; #define PG8_ROWS(x0, uidx) do { ro[x0] = (unsigned)g.rowtab[(uidx) * 256 + Rl + 64 * (x0)]; ro[(x0) + 1] = (unsigned)g.rowtab[(uidx) * 256 + Rl + 64 * (x0) + 64]; } while (0)
; #define PG8_LDA(dst, b, h) do { _Pragma("unroll") for (int m = 0; m < 4; ++m) { \
;         if constexpr (FP8) dst##8[m] = ld32(lds + PG8_SA(b, h) + aoff0 + m * 2048); \
;         else { dst[m][0] = *(const LAS bf16x8*)(lds + PG8_SA(b, h) + aoff0 + m * 2048); dst[m][1] = *(const LAS bf16x8*)(lds + PG8_SA(b, h) + aoff0 + m * 2048 + 1024); } } } while (0)
; #define PG8_LDB(dst, b, h) do { _Pragma("unroll") for (int n = 0; n < 2; ++n) { \
;         if constexpr (FP8) dst##8[n] = ld32(lds + PG8_SB(b, h) + boff0 + n * 2048); \
;         else { dst[n][0] = *(const LAS bf16x8*)(lds + PG8_SB(b, h) + boff0 + n * 2048); dst[n][1] = *(const LAS bf16x8*)(lds + PG8_SB(b, h) + boff0 + n * 2048 + 1024); } } } while (0)
; #define PG8_WAIT_V(n) asm volatile("s_waitcnt vmcnt(" #n ")" ::: "memory")
; #define PG8_WAIT_L(n) asm volatile("s_waitcnt lgkmcnt(" #n ")" ::: "memory")
;     __device__ __forceinline__ void operator()(const f32x4 (&acc)[2][2][4][2], const Unit& u, int wr, int wc, int fr, int fq) const {
;         const int row0 = u.pm * BM + wr * 64 + fr, cc = u.pn * HALF + wc * 32 + 8 * fq;
;         const float* bp = bias + (size_t)u.e * 4096 + cc;
;         f32x4 bg[2], bu[2];
; #pragma unroll
;         for (int n = 0; n < 2; ++n) { bg[n] = *(const f32x4*)(bp + 4 * n); bu[n] = *(const f32x4*)(bp + 2048 + 4 * n); }
; template <bool FP8, bool GATHER, class Epi, class Sched>
; __device__ __forceinline__ void gemm_phase(LAS unsigned char* lds, const Gemm g, const Sched& S, const Epi& E) {
;     ...
;         for (int t = 0; t < nt; t += 2) {
;             const bool last = (t == nt - 2);
;             const size_t k1 = (size_t)(t + 1) * kstep, k2 = last ? 0 : (size_t)(t + 2) * kstep, k3 = k2 + kstep;
;             const char* b2 = last ? nB : cB + (size_t)(t + 2) * kstep; const char* b3 = b2 + kstep;
;             if constexpr (GATHER) { if (last && has_next) PG8_ROWS(0, ui + 1); }
;             PG8_LDB(B0, 0, 0); PG8_SCHED; PG8_LDA(At, 0, 0); PG8_STAGEA(PG8_SA(1, 1), false, 1, k1);
;             if constexpr (GATHER) { if (last && has_next) PG8_ROWS(2, ui + 1); }
;             PG8_WAIT_V(10); PG8_WAIT_L(8); PG8_BAR; PG8_WAIT_L(0); PG8_MMA(0, 0, At, B0); PG8_BAR; PG8_SCHED;
.Llj_865:
	s_lshl_b32 s99, s36, 7
	v_lshrrev_b32_e32 v250, 1, v0
	v_and_or_b32 v250, v250, 24, s99
	v_or_b32_e32 v250, s77, v250
	v_lshlrev_b32_e32 v250, 2, v250
	s_lshl_b32 s99, s34, 14
	s_add_u32 s100, s48, s99
	s_addc_u32 s101, s49, 0
	global_load_dwordx4 v[218:221], v250, s[100:101]
	global_load_dwordx4 v[222:225], v250, s[100:101] offset:16
	s_add_u32 s90, s100, s56
	s_addc_u32 s91, s101, 0
	global_load_dwordx4 v[226:229], v250, s[90:91]
	s_add_u32 s90, s100, s14
	s_addc_u32 s91, s101, s15
	global_load_dwordx4 v[230:233], v250, s[90:91] offset:16
	s_cmp_eq_u32 s29, 12
	s_cselect_b64 s[42:43], -1, 0
	s_and_b64 s[30:31], s[38:39], s[42:43]
	v_cndmask_b32_e64 v2, 0, 1, s[30:31]
	v_cmp_ne_u32_e64 s[0:1], 1, v2
	s_andn2_b64 vcc, exec, s[30:31]
	s_cbranch_vccnz .Llj_867
	ds_read2st64_b32 v[182:183], v199 offset1:1

; #define PG8_ROWS(x0, uidx) do { ro[x0] = (unsigned)g.rowtab[(uidx) * 256 + Rl + 64 * (x0)]; ro[(x0) + 1] = (unsigned)g.rowtab[(uidx) * 256 + Rl + 64 * (x0) + 64]; } while (0)
; #define PG8_STAGE(bufoff, gbase, voff) do { _Pragma("unroll") for (int _i = 0; _i < 2; ++_i) \
;         __builtin_amdgcn_global_load_lds((const unsigned*)(sbase((const char*)(gbase) + _i * pstep) + (voff)), (LAS unsigned*)(lds + (bufoff) + ldsw + _i * 8192), 16, 0, 0); } while (0)
; #define PG8_LDA(dst, b, h) do { _Pragma("unroll") for (int m = 0; m < 4; ++m) { \
;         if constexpr (FP8) dst##8[m] = ld32(lds + PG8_SA(b, h) + aoff0 + m * 2048); \
;         else { dst[m][0] = *(const LAS bf16x8*)(lds + PG8_SA(b, h) + aoff0 + m * 2048); dst[m][1] = *(const LAS bf16x8*)(lds + PG8_SA(b, h) + aoff0 + m * 2048 + 1024); } } } while (0)
; #define PG8_LDB(dst, b, h) do { _Pragma("unroll") for (int n = 0; n < 2; ++n) { \
;         if constexpr (FP8) dst##8[n] = ld32(lds + PG8_SB(b, h) + boff0 + n * 2048); \
;         else { dst[n][0] = *(const LAS bf16x8*)(lds + PG8_SB(b, h) + boff0 + n * 2048); dst[n][1] = *(const LAS bf16x8*)(lds + PG8_SB(b, h) + boff0 + n * 2048 + 1024); } } } while (0)
; #define PG8_WAIT_V(n) asm volatile("s_waitcnt vmcnt(" #n ")" ::: "memory")
; template <bool FP8, bool GATHER, class Epi, class Sched>
; __device__ __forceinline__ void gemm_phase(LAS unsigned char* lds, const Gemm g, const Sched& S, const Epi& E) {
;     ...
;             PG8_LDB(B0, 0, 0); PG8_SCHED; PG8_LDA(At, 0, 0); PG8_STAGEA(PG8_SA(1, 1), false, 1, k1);
;             if constexpr (GATHER) { if (last && has_next) PG8_ROWS(2, ui + 1); }
;             PG8_WAIT_V(10); PG8_WAIT_L(8); PG8_BAR; PG8_WAIT_L(0); PG8_MMA(0, 0, At, B0); PG8_BAR; PG8_SCHED;
;             PG8_LDB(B1, 0, 1); PG8_STAGE(PG8_SB(0, 0), b2, voffB);
;             PG8_WAIT_V(10); PG8_BAR; PG8_WAIT_L(0); PG8_MMA(0, 1, At, B1); PG8_BAR;
;             PG8_LDA(At, 0, 1); PG8_STAGEA(PG8_SA(0, 0), last, 0, k2);
;             PG8_BAR; PG8_WAIT_L(0); if (cfull) PG8_MMA(1, 0, At, B0); PG8_BAR; PG8_SCHED;
;             PG8_STAGE(PG8_SB(0, 1), b2 + hstep, voffB);
;             PG8_WAIT_V(10); PG8_BAR; if (cfull) PG8_MMA(1, 1, At, B1); PG8_BAR;
;             PG8_LDB(B0, 1, 0); PG8_SCHED; PG8_LDA(At, 1, 0); PG8_STAGEA(PG8_SA(0, 1), last, 1, k2);
;             PG8_WAIT_V(10); PG8_WAIT_L(8); PG8_BAR; PG8_WAIT_L(0); PG8_MMA(0, 0, At, B0); PG8_BAR; PG8_SCHED;
.Llj_869:
	s_add_u32 s0, s40, 0x100
	s_addc_u32 s1, s41, 0
	s_and_b64 s[30:31], s[42:43], exec
	s_cselect_b32 s2, 0, s0
	s_add_u32 s33, s25, s40
	s_addc_u32 s35, s28, s41
	s_waitcnt vmcnt(14)
	s_and_b64 s[30:31], s[42:43], exec
	s_waitcnt lgkmcnt(8)
	s_barrier
	s_waitcnt lgkmcnt(0)
	s_cselect_b32 s40, s19, s33
	s_cselect_b32 s41, s17, s35
	s_add_u32 s42, s40, 0x80
	v_mov_b32_e32 v187, v181
	s_addc_u32 s43, s41, 0
	s_setprio 1
	s_waitcnt lgkmcnt(0)
	v_mfma_f32_16x16x128_f8f6f4 v[174:177], v[2:9], v[42:49], v[174:177]
	v_mfma_f32_16x16x128_f8f6f4 v[166:169], v[10:17], v[42:49], v[166:169]
	v_mfma_f32_16x16x128_f8f6f4 v[158:161], v[2:9], v[34:41], v[158:161]
	v_mfma_f32_16x16x128_f8f6f4 v[150:153], v[10:17], v[34:41], v[150:153]
	v_mfma_f32_16x16x128_f8f6f4 v[142:145], v[2:9], v[26:33], v[142:145]
	v_mfma_f32_16x16x128_f8f6f4 v[134:137], v[10:17], v[26:33], v[134:137]
	v_mfma_f32_16x16x128_f8f6f4 v[126:129], v[2:9], v[18:25], v[126:129]
	v_mfma_f32_16x16x128_f8f6f4 v[118:121], v[10:17], v[18:25], v[118:121]
	s_setprio 0
	s_barrier
	s_add_i32 s33, 0, 0x14000
	v_add_u32_e32 v212, s33, v197
	s_mov_b64 s[30:31], s[40:41]
	ds_read_b128 v[200:203], v212
	ds_read_b128 v[204:207], v212 offset:1024
	ds_read_b128 v[208:211], v212 offset:2048
	ds_read_b128 v[212:215], v212 offset:3072
	s_mov_b32 m0, s63
	v_lshl_add_u64 v[216:217], s[30:31], 0, v[178:179]
	s_add_u32 s30, s40, 0x20000
	s_addc_u32 s31, s41, 0
	global_load_lds_dwordx4 v[216:217], off
	s_mov_b32 m0, s64
	v_lshl_add_u64 v[216:217], s[30:31], 0, v[178:179]
	global_load_lds_dwordx4 v[216:217], off
	s_waitcnt vmcnt(14)
	s_barrier
	s_waitcnt lgkmcnt(0)
	s_setprio 1
	s_waitcnt lgkmcnt(0)
	v_mfma_f32_16x16x128_f8f6f4 v[170:173], v[200:207], v[42:49], v[170:173]
	v_mfma_f32_16x16x128_f8f6f4 v[162:165], v[208:215], v[42:49], v[162:165]
	v_mfma_f32_16x16x128_f8f6f4 v[154:157], v[200:207], v[34:41], v[154:157]
	v_mfma_f32_16x16x128_f8f6f4 v[146:149], v[208:215], v[34:41], v[146:149]
	v_mfma_f32_16x16x128_f8f6f4 v[138:141], v[200:207], v[26:33], v[138:141]
	v_mfma_f32_16x16x128_f8f6f4 v[130:133], v[208:215], v[26:33], v[130:133]
	v_mfma_f32_16x16x128_f8f6f4 v[122:125], v[200:207], v[18:25], v[122:125]
	v_mfma_f32_16x16x128_f8f6f4 v[114:117], v[208:215], v[18:25], v[114:117]
	s_setprio 0
	s_add_u32 s44, s4, s2
	s_addc_u32 s45, s5, 0
	s_mov_b64 s[30:31], s[44:45]
	s_mov_b32 m0, s37
	s_barrier
	ds_read_b128 v[18:21], v198 offset:16384
	ds_read_b128 v[22:25], v198 offset:17408
	ds_read_b128 v[26:29], v198 offset:18432
	ds_read_b128 v[30:33], v198 offset:19456
	ds_read_b128 v[34:37], v198 offset:20480
	ds_read_b128 v[38:41], v198 offset:21504
	ds_read_b128 v[42:45], v198 offset:22528
	ds_read_b128 v[46:49], v198 offset:23552
	v_add_u32_e32 v216, v182, v191
	global_load_lds_dwordx4 v216, s[30:31]
	s_mov_b64 s[30:31], s[44:45]
	v_add_u32_e32 v217, v183, v191
	s_mov_b32 m0, s65
	s_nop 0
	global_load_lds_dwordx4 v217, s[30:31]
	s_barrier
	s_waitcnt lgkmcnt(0)
	s_setprio 1
	s_waitcnt lgkmcnt(0)
	v_mfma_f32_16x16x128_f8f6f4 v[110:113], v[2:9], v[18:25], v[110:113]
	v_mfma_f32_16x16x128_f8f6f4 v[102:105], v[10:17], v[18:25], v[102:105]
	v_mfma_f32_16x16x128_f8f6f4 v[94:97], v[2:9], v[26:33], v[94:97]
	v_mfma_f32_16x16x128_f8f6f4 v[86:89], v[10:17], v[26:33], v[86:89]
	v_mfma_f32_16x16x128_f8f6f4 v[78:81], v[2:9], v[34:41], v[78:81]
	v_mfma_f32_16x16x128_f8f6f4 v[70:73], v[10:17], v[34:41], v[70:73]
	v_mfma_f32_16x16x128_f8f6f4 v[62:65], v[2:9], v[42:49], v[62:65]
	v_mfma_f32_16x16x128_f8f6f4 v[54:57], v[10:17], v[42:49], v[54:57]
	s_setprio 0
	s_barrier
	s_add_u32 s30, s40, 0x40000
	s_addc_u32 s31, s41, 0
	s_add_i32 s2, s33, s62
	v_lshl_add_u64 v[2:3], s[30:31], 0, v[178:179]
	s_add_u32 s30, s40, 0x60000
	s_mov_b32 m0, s2
	s_addc_u32 s31, s41, 0
	global_load_lds_dwordx4 v[2:3], off
	s_add_i32 m0, s2, 0x2000
	v_lshl_add_u64 v[2:3], s[30:31], 0, v[178:179]
	global_load_lds_dwordx4 v[2:3], off
	s_waitcnt vmcnt(14)
	s_barrier
	s_setprio 1
	v_mfma_f32_16x16x128_f8f6f4 v[106:109], v[200:207], v[18:25], v[106:109]
	v_mfma_f32_16x16x128_f8f6f4 v[98:101], v[208:215], v[18:25], v[98:101]
	v_mfma_f32_16x16x128_f8f6f4 v[90:93], v[200:207], v[26:33], v[90:93]
	v_mfma_f32_16x16x128_f8f6f4 v[82:85], v[208:215], v[26:33], v[82:85]
	v_mfma_f32_16x16x128_f8f6f4 v[74:77], v[200:207], v[34:41], v[74:77]
	v_mfma_f32_16x16x128_f8f6f4 v[66:69], v[208:215], v[34:41], v[66:69]
	v_mfma_f32_16x16x128_f8f6f4 v[58:61], v[200:207], v[42:49], v[58:61]
	v_mfma_f32_16x16x128_f8f6f4 v[50:53], v[208:215], v[42:49], v[50:53]
	s_setprio 0
	s_add_i32 s2, 0, 0x18000
	v_add_u32_e32 v14, s2, v197
	s_barrier
	ds_read_b128 v[2:5], v14
	ds_read_b128 v[6:9], v14 offset:1024
	ds_read_b128 v[10:13], v14 offset:2048
	ds_read_b128 v[14:17], v14 offset:3072
	s_mov_b64 s[30:31], s[44:45]
	ds_read_b128 v[18:21], v198 offset:32768
	ds_read_b128 v[22:25], v198 offset:33792
	ds_read_b128 v[26:29], v198 offset:34816
	ds_read_b128 v[30:33], v198 offset:35840
	ds_read_b128 v[34:37], v198 offset:36864
	ds_read_b128 v[38:41], v198 offset:37888
	ds_read_b128 v[42:45], v198 offset:38912
	ds_read_b128 v[46:49], v198 offset:39936
	s_mov_b32 m0, s66
	v_lshl_add_u64 v[200:201], s[30:31], 0, v[180:181]
	s_mov_b64 s[30:31], s[44:45]
	global_load_lds_dwordx4 v[200:201], off
	s_mov_b32 m0, s67
	v_lshl_add_u64 v[186:187], s[30:31], 0, v[186:187]
	global_load_lds_dwordx4 v[186:187], off
	s_waitcnt vmcnt(14)
	s_waitcnt lgkmcnt(8)
	s_barrier
; #define PG8_STAGE(bufoff, gbase, voff) do { _Pragma("unroll") for (int _i = 0; _i < 2; ++_i) \
;         __builtin_amdgcn_global_load_lds((const unsigned*)(sbase((const char*)(gbase) + _i * pstep) + (voff)), (LAS unsigned*)(lds + (bufoff) + ldsw + _i * 8192), 16, 0, 0); } while (0)
; #define PG8_LDA(dst, b, h) do { _Pragma("unroll") for (int m = 0; m < 4; ++m) { \
;         if constexpr (FP8) dst##8[m] = ld32(lds + PG8_SA(b, h) + aoff0 + m * 2048); \
;         else { dst[m][0] = *(const LAS bf16x8*)(lds + PG8_SA(b, h) + aoff0 + m * 2048); dst[m][1] = *(const LAS bf16x8*)(lds + PG8_SA(b, h) + aoff0 + m * 2048 + 1024); } } } while (0)
; #define PG8_LDB(dst, b, h) do { _Pragma("unroll") for (int n = 0; n < 2; ++n) { \
;         if constexpr (FP8) dst##8[n] = ld32(lds + PG8_SB(b, h) + boff0 + n * 2048); \
;         else { dst[n][0] = *(const LAS bf16x8*)(lds + PG8_SB(b, h) + boff0 + n * 2048); dst[n][1] = *(const LAS bf16x8*)(lds + PG8_SB(b, h) + boff0 + n * 2048 + 1024); } } } while (0)
; #define PG8_WAIT_V(n) asm volatile("s_waitcnt vmcnt(" #n ")" ::: "memory")
; #define PG8_WAIT_L(n) asm volatile("s_waitcnt lgkmcnt(" #n ")" ::: "memory")
;     __device__ __forceinline__ void operator()(const f32x4 (&acc)[2][2][4][2], const Unit& u, int wr, int wc, int fr, int fq) const {
;         const int row0 = u.pm * BM + wr * 64 + fr, cc = u.pn * HALF + wc * 32 + 8 * fq;
;         const float* bp = bias + (size_t)u.e * 4096 + cc;
;         f32x4 bg[2], bu[2];
; #pragma unroll
;         for (int n = 0; n < 2; ++n) { bg[n] = *(const f32x4*)(bp + 4 * n); bu[n] = *(const f32x4*)(bp + 2048 + 4 * n); }
; template <bool FP8, bool GATHER, class Epi, class Sched>
; __device__ __forceinline__ void gemm_phase(LAS unsigned char* lds, const Gemm g, const Sched& S, const Epi& E) {
;     ...
;             PG8_WAIT_V(10); PG8_WAIT_L(8); PG8_BAR; PG8_WAIT_L(0); PG8_MMA(0, 0, At, B0); PG8_BAR; PG8_SCHED;
;             PG8_LDB(B1, 1, 1); PG8_STAGE(PG8_SB(1, 0), b3, voffB);
;             PG8_WAIT_V(10); PG8_BAR; PG8_WAIT_L(0); PG8_MMA(0, 1, At, B1); PG8_BAR;
;             PG8_LDA(At, 1, 1); PG8_STAGEA(PG8_SA(1, 0), last, 0, k3);
;             PG8_BAR; PG8_WAIT_L(0); if (cfull) PG8_MMA(1, 0, At, B0); PG8_BAR; PG8_SCHED;
;             PG8_STAGE(PG8_SB(1, 1), b3 + hstep, voffB);
;             PG8_WAIT_V(10); PG8_BAR; if (cfull) PG8_MMA(1, 1, At, B1); PG8_BAR;
	s_waitcnt lgkmcnt(0)
	s_setprio 1
	s_waitcnt lgkmcnt(0)
	v_mfma_f32_16x16x128_f8f6f4 v[174:177], v[2:9], v[18:25], v[174:177]
	v_mfma_f32_16x16x128_f8f6f4 v[166:169], v[10:17], v[18:25], v[166:169]
	v_mfma_f32_16x16x128_f8f6f4 v[158:161], v[2:9], v[26:33], v[158:161]
	v_mfma_f32_16x16x128_f8f6f4 v[150:153], v[10:17], v[26:33], v[150:153]
	v_mfma_f32_16x16x128_f8f6f4 v[142:145], v[2:9], v[34:41], v[142:145]
	v_mfma_f32_16x16x128_f8f6f4 v[134:137], v[10:17], v[34:41], v[134:137]
	v_mfma_f32_16x16x128_f8f6f4 v[126:129], v[2:9], v[42:49], v[126:129]
	v_mfma_f32_16x16x128_f8f6f4 v[118:121], v[10:17], v[42:49], v[118:121]
	s_setprio 0
	s_barrier
	s_add_i32 s33, 0, 0x1c000
	s_add_i32 s2, s2, s62
	v_add_u32_e32 v180, s33, v197
	s_add_u32 s30, s40, 0x20080
	ds_read_b128 v[200:203], v180
	ds_read_b128 v[204:207], v180 offset:1024
	ds_read_b128 v[208:211], v180 offset:2048
	ds_read_b128 v[212:215], v180 offset:3072
	s_mov_b32 m0, s2
	v_lshl_add_u64 v[186:187], s[42:43], 0, v[178:179]
	s_addc_u32 s31, s41, 0
	global_load_lds_dwordx4 v[186:187], off
	s_add_i32 m0, s2, 0x2000
	v_lshl_add_u64 v[186:187], s[30:31], 0, v[178:179]
	global_load_lds_dwordx4 v[186:187], off
	s_waitcnt vmcnt(10)
	s_barrier
	s_waitcnt lgkmcnt(0)
	s_setprio 1
	s_waitcnt lgkmcnt(0)
	v_mfma_f32_16x16x128_f8f6f4 v[170:173], v[200:207], v[18:25], v[170:173]
	v_mfma_f32_16x16x128_f8f6f4 v[162:165], v[208:215], v[18:25], v[162:165]
	v_mfma_f32_16x16x128_f8f6f4 v[154:157], v[200:207], v[26:33], v[154:157]
	v_mfma_f32_16x16x128_f8f6f4 v[146:149], v[208:215], v[26:33], v[146:149]
	v_mfma_f32_16x16x128_f8f6f4 v[138:141], v[200:207], v[34:41], v[138:141]
	v_mfma_f32_16x16x128_f8f6f4 v[130:133], v[208:215], v[34:41], v[130:133]
	v_mfma_f32_16x16x128_f8f6f4 v[122:125], v[200:207], v[42:49], v[122:125]
	v_mfma_f32_16x16x128_f8f6f4 v[114:117], v[208:215], v[42:49], v[114:117]
	s_setprio 0
	s_add_u32 s30, s44, 0x80
	s_addc_u32 s31, s45, 0
	s_mov_b64 s[42:43], s[30:31]
	s_mov_b32 m0, s78
	s_barrier
	ds_read_b128 v[18:21], v198 offset:49152
	ds_read_b128 v[22:25], v198 offset:50176
	ds_read_b128 v[26:29], v198 offset:51200
	ds_read_b128 v[30:33], v198 offset:52224
	ds_read_b128 v[34:37], v198 offset:53248
	ds_read_b128 v[38:41], v198 offset:54272
	ds_read_b128 v[42:45], v198 offset:55296
	ds_read_b128 v[46:49], v198 offset:56320
	s_nop 0
	global_load_lds_dwordx4 v216, s[42:43]
	s_mov_b32 m0, s79
	s_nop 0
	global_load_lds_dwordx4 v217, s[30:31]
	s_barrier
	s_waitcnt lgkmcnt(0)
	s_setprio 1
	s_waitcnt lgkmcnt(0)
	v_mfma_f32_16x16x128_f8f6f4 v[110:113], v[2:9], v[18:25], v[110:113]
	v_mfma_f32_16x16x128_f8f6f4 v[102:105], v[10:17], v[18:25], v[102:105]
	v_mfma_f32_16x16x128_f8f6f4 v[94:97], v[2:9], v[26:33], v[94:97]
	v_mfma_f32_16x16x128_f8f6f4 v[86:89], v[10:17], v[26:33], v[86:89]
	v_mfma_f32_16x16x128_f8f6f4 v[78:81], v[2:9], v[34:41], v[78:81]
	v_mfma_f32_16x16x128_f8f6f4 v[70:73], v[10:17], v[34:41], v[70:73]
	v_mfma_f32_16x16x128_f8f6f4 v[62:65], v[2:9], v[42:49], v[62:65]
	v_mfma_f32_16x16x128_f8f6f4 v[54:57], v[10:17], v[42:49], v[54:57]
	s_setprio 0
	s_barrier
	s_add_u32 s30, s40, 0x40080
	s_addc_u32 s31, s41, 0
	s_add_i32 s2, s33, s62
	v_lshl_add_u64 v[2:3], s[30:31], 0, v[178:179]
	s_add_u32 s30, s40, 0x60080
	s_mov_b32 m0, s2
	s_addc_u32 s31, s41, 0
	global_load_lds_dwordx4 v[2:3], off
	s_add_i32 m0, s2, 0x2000
	v_lshl_add_u64 v[2:3], s[30:31], 0, v[178:179]
	global_load_lds_dwordx4 v[2:3], off
	s_waitcnt vmcnt(10)
	s_barrier
	s_setprio 1
	v_mfma_f32_16x16x128_f8f6f4 v[106:109], v[200:207], v[18:25], v[106:109]
	v_mfma_f32_16x16x128_f8f6f4 v[98:101], v[208:215], v[18:25], v[98:101]
	v_mfma_f32_16x16x128_f8f6f4 v[90:93], v[200:207], v[26:33], v[90:93]
	v_mfma_f32_16x16x128_f8f6f4 v[82:85], v[208:215], v[26:33], v[82:85]
	v_mfma_f32_16x16x128_f8f6f4 v[74:77], v[200:207], v[34:41], v[74:77]
	v_mfma_f32_16x16x128_f8f6f4 v[66:69], v[208:215], v[34:41], v[66:69]
	v_mfma_f32_16x16x128_f8f6f4 v[58:61], v[200:207], v[42:49], v[58:61]
	v_mfma_f32_16x16x128_f8f6f4 v[50:53], v[208:215], v[42:49], v[50:53]
	s_setprio 0
	s_mov_b32 s82, 4
	s_add_i32 s29, s29, 2
	s_cmp_gt_u32 s29, 13
	s_barrier
	s_cbranch_scc1 .LBB0_853
	s_mov_b64 s[40:41], s[0:1]
	s_branch .LBB0_865
.Lbp_pre:
	v_and_or_b32 v18, v18, 15, s76
	v_lshl_add_u32 v22, s24, 8, v18
	s_mov_b32 s34, s16
	s_mov_b32 s36, s18
	s_mov_b32 s24, s81
	s_mov_b64 s[0:1], s[20:21]
	v_mov_b32_e32 v14, v218
	v_mov_b32_e32 v15, v219
	v_mov_b32_e32 v16, v220
	v_mov_b32_e32 v17, v221
	v_mov_b32_e32 v6, v222
	v_mov_b32_e32 v7, v223
	v_mov_b32_e32 v8, v224
	v_mov_b32_e32 v9, v225
	v_mov_b32_e32 v10, v226
	v_mov_b32_e32 v11, v227
	v_mov_b32_e32 v12, v228
	v_mov_b32_e32 v13, v229
	v_mov_b32_e32 v2, v230
	v_mov_b32_e32 v3, v231
	v_mov_b32_e32 v4, v232
	v_mov_b32_e32 v5, v233
	s_lshr_b32 s90, s98, 1
	s_mul_i32 s90, s90, s83
	s_add_i32 s90, s90, s84
	s_cmp_lt_u32 s90, 0x8000
	s_cbranch_scc0 .Lbp_no
	s_lshr_b32 s91, s90, 10
	s_lshl_b32 s91, s91, 11
	s_and_b32 s99, s90, 0x3c0
	s_lshl_b32 s99, s99, 1
	s_or_b32 s91, s91, s99
	s_and_b32 s99, s98, 1
	s_lshl_b32 s99, s99, 6
	s_or_b32 s91, s91, s99
	s_and_b32 s90, s90, 63
	s_or_b32 s90, s90, s91
	s_lshr_b32 s91, s90, 11
	s_and_b32 s99, s90, 0x7c0
	s_and_b32 s82, s90, 63
	s_lshl_b32 s32, s91, 24
	s_lshl_b32 s100, s99, 13
	s_add_i32 s32, s32, s100
	s_lshl_b32 s100, s82, 7
	s_add_i32 s32, s32, s100
	s_add_u32 s100, s86, s32
	s_addc_u32 s101, s87, 0
	s_lshl_b32 s32, s91, 22
	s_lshl_b32 s82, s82, 16
	s_add_i32 s32, s32, s82
	s_add_i32 s32, s32, s99
	s_add_u32 s90, s88, s32
	s_addc_u32 s91, s89, 0
	global_load_dwordx4 v[218:221], v252, s[100:101] nt
	s_add_u32 s100, s100, 0x2000
	s_addc_u32 s101, s101, 0
	global_load_dwordx4 v[222:225], v252, s[100:101] nt
	s_add_u32 s100, s100, 0x2000
	s_addc_u32 s101, s101, 0
	global_load_dwordx4 v[226:229], v252, s[100:101] nt
	s_add_u32 s100, s100, 0x2000
	s_addc_u32 s101, s101, 0
	global_load_dwordx4 v[230:233], v252, s[100:101] nt
	s_add_u32 s100, s100, 0x2000
	s_addc_u32 s101, s101, 0
	global_load_dwordx4 v[234:237], v252, s[100:101] nt
	s_add_u32 s100, s100, 0x2000
	s_addc_u32 s101, s101, 0
	global_load_dwordx4 v[238:241], v252, s[100:101] nt
	s_add_u32 s100, s100, 0x2000
	s_addc_u32 s101, s101, 0
	global_load_dwordx4 v[242:245], v252, s[100:101] nt
	s_add_u32 s100, s100, 0x2000
	s_addc_u32 s101, s101, 0
	global_load_dwordx4 v[246:249], v252, s[100:101] nt
	s_mov_b32 s82, 1
	s_waitcnt vmcnt(8)
	s_branch .Lesj_join
.Lbp_no:
	s_mov_b32 s82, 0
	s_waitcnt vmcnt(0)
	s_branch .Lesj_join
